# attention: offset-table LDS read hoisted above the per-stage barrier in the selected and window loops
# baseline (speedup 1.0000x reference)
.LBB0_1120:
	s_mov_b32 s98, 0x26000
	v_lshl_add_u32 v118, v0, 4, s98
	ds_read_b128 v[118:121], v118
	s_add_u32 s6, s13, s96
	s_add_i32 s0, s6, 1
	s_cmp_ge_i32 s0, s12
	s_mov_b64 s[0:1], -1
	s_cbranch_scc0 .LBB0_1122
	s_waitcnt vmcnt(0)
	s_mov_b64 s[0:1], 0

.LBB0_1132:
	s_mul_hi_u32 s1, s47, 0xaaaaaaab
	s_lshr_b32 s1, s1, 1
	s_mul_i32 s1, s1, 0x18000
	s_sub_i32 s21, s64, s1
	s_sub_i32 s38, s80, s1
	s_sub_i32 s39, s79, s1
	s_sub_i32 s1, s58, s1
	s_mul_i32 s6, s0, s42
	s_lshl_b32 s6, s6, 1
	s_add_u32 s98, s34, s6
	s_addc_u32 s99, s35, 0
	s_lshl_b32 s6, s0, 1
	s_add_u32 s100, s18, s6
	s_addc_u32 s101, s19, 0
	s_add_i32 s1, s8, s1
	s_add_i32 m0, s9, s1
	s_waitcnt lgkmcnt(0)
	global_load_lds_dwordx4 v118, s[98:99]
	s_add_i32 s1, s8, s38
	s_add_i32 m0, s9, s1
	s_nop 0
	global_load_lds_dwordx4 v119, s[98:99]
	s_add_i32 s6, s8, s39
	s_add_i32 m0, s9, s6
	s_nop 0
	global_load_lds_dwordx4 v120, s[100:101]
	s_add_i32 s0, s8, s21
	s_add_i32 m0, s9, s0
	s_nop 0
	global_load_lds_dwordx4 v121, s[100:101]
.LBB0_1133:
	s_waitcnt lgkmcnt(0)
	s_sub_i32 s6, s96, 64
	s_lshr_b64 s[18:19], s[26:27], s96
	s_lshr_b64 s[20:21], s[28:29], s6
	s_lshr_b64 s[34:35], s[22:23], s96
	s_lshr_b64 s[38:39], s[24:25], s6
	s_cmp_lt_u32 s96, 64
	s_cselect_b64 s[0:1], -1, 0
	s_and_b64 s[42:43], s[0:1], exec
	s_cselect_b32 s7, s18, s20
	s_cselect_b32 s20, s34, s38
	s_bitcmp1_b32 s7, 0
	s_cselect_b64 s[18:19], -1, 0
	s_bitcmp1_b32 s20, 0
	s_cselect_b64 s[76:77], -1, 0
	s_or_b64 s[20:21], s[18:19], s[76:77]
	s_andn2_b64 vcc, exec, s[20:21]
	s_cbranch_vccnz .LBB0_1139
	v_lshrrev_b64 v[118:119], s96, v[200:201]
	v_lshrrev_b64 v[120:121], s6, v[202:203]
	v_cndmask_b32_e64 v2, v120, v118, s[0:1]
	v_lshrrev_b64 v[118:119], s96, v[196:197]
	v_lshrrev_b64 v[120:121], s6, v[198:199]
	v_cndmask_b32_e64 v1, v120, v118, s[0:1]
	s_mul_hi_u32 s0, s50, 0xaaaaaaab
	s_lshr_b32 s34, s0, 1
	s_and_b64 s[6:7], s[18:19], s[76:77]
	s_cmpk_lt_i32 s45, 0x7f
	s_cselect_b64 s[0:1], -1, 0
	s_cmpk_gt_i32 s45, 0x7e
	s_cselect_b64 s[20:21], -1, 0
	s_mul_i32 s34, s34, 0x18000
	s_and_b64 s[20:21], s[20:21], s[6:7]
	v_cndmask_b32_e64 v5, 0, 1, s[18:19]
	v_subrev_u32_e32 v142, s34, v232
	v_subrev_u32_e32 v143, s34, v233
	v_subrev_u32_e32 v144, s34, v234
	v_subrev_u32_e32 v145, s34, v235
	s_mov_b64 s[6:7], -1
	s_andn2_b64 vcc, exec, s[20:21]
	v_cmp_ne_u32_e64 s[18:19], 1, v5
	s_cbranch_vccz .LBB0_1160
	s_and_b64 vcc, exec, s[18:19]
	v_mov_b64_e32 v[204:205], v[136:137]
	v_mov_b64_e32 v[206:207], v[134:135]
	s_cbranch_vccnz .LBB0_1147
	s_add_i32 s6, s9, s8
	v_add_u32_e32 v5, s6, v145
	v_add_u32_e32 v150, s6, v144
	v_add_u32_e32 v151, s6, v143
	v_add_u32_e32 v154, s6, v142
	ds_read_b128 v[38:41], v5
	ds_read_b128 v[42:45], v5 offset:4096
	ds_read_b128 v[118:121], v150
	ds_read_b128 v[122:125], v150 offset:4096
	ds_read_b128 v[126:129], v151
	ds_read_b128 v[138:141], v151 offset:4096
	ds_read_b128 v[130:133], v154
	ds_read_b128 v[146:149], v154 offset:4096
	s_setprio 1
	s_waitcnt lgkmcnt(0)
	v_mfma_f32_16x16x32_f16 v[38:41], v[38:41], v[6:9], 0
	v_mfma_f32_16x16x32_f16 v[38:41], v[118:121], v[10:13], v[38:41]
	v_mfma_f32_16x16x32_f16 v[38:41], v[126:129], v[14:17], v[38:41]
	v_mfma_f32_16x16x32_f16 v[130:133], v[130:133], v[18:21], v[38:41]
	v_mfma_f32_16x16x32_f16 v[38:41], v[42:45], v[6:9], 0
	v_mfma_f32_16x16x32_f16 v[38:41], v[122:125], v[10:13], v[38:41]
	v_mfma_f32_16x16x32_f16 v[38:41], v[138:141], v[14:17], v[38:41]
	v_mfma_f32_16x16x32_f16 v[126:129], v[146:149], v[18:21], v[38:41]
	s_setprio 0
	s_nop 5
	ds_read_b128 v[38:41], v5 offset:8192
	ds_read_b128 v[42:45], v5 offset:12288
	ds_read_b128 v[118:121], v150 offset:8192
	ds_read_b128 v[138:141], v150 offset:12288
	ds_read_b128 v[122:125], v151 offset:8192
	ds_read_b128 v[146:149], v151 offset:12288
	ds_read_b128 v[150:153], v154 offset:8192
	ds_read_b128 v[154:157], v154 offset:12288
	s_setprio 1
	s_waitcnt lgkmcnt(0)
	v_mfma_f32_16x16x32_f16 v[38:41], v[38:41], v[6:9], 0
	v_mfma_f32_16x16x32_f16 v[38:41], v[118:121], v[10:13], v[38:41]
	v_mfma_f32_16x16x32_f16 v[38:41], v[122:125], v[14:17], v[38:41]
	v_mfma_f32_16x16x32_f16 v[122:125], v[150:153], v[18:21], v[38:41]
	v_mfma_f32_16x16x32_f16 v[38:41], v[42:45], v[6:9], 0
	v_mfma_f32_16x16x32_f16 v[38:41], v[138:141], v[10:13], v[38:41]
	v_mfma_f32_16x16x32_f16 v[38:41], v[146:149], v[14:17], v[38:41]
	v_mfma_f32_16x16x32_f16 v[118:121], v[154:157], v[18:21], v[38:41]
	s_setprio 0
	s_mov_b64 s[6:7], -1
	s_and_b64 vcc, exec, s[0:1]
	s_cbranch_vccz .LBB0_1142
	v_add_u32_e32 v5, s45, v238
	s_nop 1
	v_add_u32_e32 v38, 63, v5
	v_add_u32_e32 v40, 62, v5
	v_add_u32_e32 v42, 61, v5
	v_add_u32_e32 v44, 60, v5
	v_add_u32_e32 v138, 59, v5
	v_add_u32_e32 v140, 58, v5
	v_add_u32_e32 v146, 57, v5
	v_add_u32_e32 v148, 56, v5
	v_add_u32_e32 v150, 31, v5
	v_add_u32_e32 v152, 30, v5
	v_add_u32_e32 v154, 29, v5
	v_add_u32_e32 v156, 28, v5
	v_add_u32_e32 v158, 27, v5
	v_add_u32_e32 v160, 26, v5
	v_add_u32_e32 v162, 25, v5
	v_med3_i32 v39, v38, 0, v243
	v_med3_i32 v41, v40, 0, v243
	v_med3_i32 v43, v42, 0, v243
	v_med3_i32 v45, v44, 0, v243
	v_med3_i32 v139, v138, 0, v243
	v_med3_i32 v141, v140, 0, v243
	v_med3_i32 v147, v146, 0, v243
	v_med3_i32 v149, v148, 0, v243
	v_med3_i32 v151, v150, 0, v243
	v_med3_i32 v153, v152, 0, v243
	v_med3_i32 v155, v154, 0, v243
	v_med3_i32 v157, v156, 0, v243
	v_med3_i32 v159, v158, 0, v243
	v_med3_i32 v161, v160, 0, v243
	v_med3_i32 v163, v162, 0, v243
	v_add_u32_e32 v164, 24, v5
	v_lshl_add_u32 v39, v39, 2, v244
	v_lshl_add_u32 v41, v41, 2, v244
	v_lshl_add_u32 v43, v43, 2, v244
	v_lshl_add_u32 v45, v45, 2, v244
	v_lshl_add_u32 v139, v139, 2, v244
	v_lshl_add_u32 v141, v141, 2, v244
	v_lshl_add_u32 v147, v147, 2, v244
	v_lshl_add_u32 v149, v149, 2, v244
	v_lshl_add_u32 v151, v151, 2, v244
	v_lshl_add_u32 v153, v153, 2, v244
	v_lshl_add_u32 v155, v155, 2, v244
	v_lshl_add_u32 v157, v157, 2, v244
	v_lshl_add_u32 v159, v159, 2, v244
	v_lshl_add_u32 v161, v161, 2, v244
	v_lshl_add_u32 v163, v163, 2, v244
	v_med3_i32 v5, v164, 0, v243
	ds_read_b32 v39, v39
	ds_read_b32 v41, v41
	ds_read_b32 v43, v43
	ds_read_b32 v45, v45
	ds_read_b32 v139, v139
	ds_read_b32 v141, v141
	ds_read_b32 v147, v147
	ds_read_b32 v149, v149
	v_lshl_add_u32 v5, v5, 2, v244
	ds_read_b32 v151, v151
	ds_read_b32 v153, v153
	ds_read_b32 v155, v155
	ds_read_b32 v157, v157
	ds_read_b32 v159, v159
	ds_read_b32 v161, v161
	ds_read_b32 v163, v163
	ds_read_b32 v165, v5
	v_and_b32_e32 v5, 1, v2
	v_cmp_eq_u32_e32 vcc, 1, v5
	v_cmp_lt_i32_e64 s[0:1], -1, v38
	s_waitcnt lgkmcnt(0)
	v_fmac_f32_e32 v39, 0x3e0293ee, v130
	s_and_b64 s[0:1], s[0:1], vcc
	v_cndmask_b32_e64 v5, v241, v39, s[0:1]
	v_cmp_lt_i32_e64 s[0:1], -1, v40
	v_fmac_f32_e32 v41, 0x3e0293ee, v131
	s_and_b64 s[0:1], s[0:1], vcc
	v_cndmask_b32_e64 v38, v241, v41, s[0:1]
	v_cmp_lt_i32_e64 s[0:1], -1, v42
	v_fmac_f32_e32 v43, 0x3e0293ee, v132
	s_and_b64 s[0:1], s[0:1], vcc
	v_cndmask_b32_e64 v39, v241, v43, s[0:1]
	v_cmp_lt_i32_e64 s[0:1], -1, v44
	v_fmac_f32_e32 v45, 0x3e0293ee, v133
	s_and_b64 s[0:1], s[0:1], vcc
	v_cndmask_b32_e64 v41, v241, v45, s[0:1]
	v_cmp_lt_i32_e64 s[0:1], -1, v138
	v_fmac_f32_e32 v139, 0x3e0293ee, v126
	s_and_b64 s[0:1], s[0:1], vcc
	v_cndmask_b32_e64 v40, v241, v139, s[0:1]
	v_cmp_lt_i32_e64 s[0:1], -1, v140
	v_fmac_f32_e32 v141, 0x3e0293ee, v127
	s_and_b64 s[0:1], s[0:1], vcc
	v_cndmask_b32_e64 v140, v241, v141, s[0:1]
	v_cmp_lt_i32_e64 s[0:1], -1, v146
	v_fmac_f32_e32 v147, 0x3e0293ee, v128
	s_and_b64 s[0:1], s[0:1], vcc
	v_cndmask_b32_e64 v147, v241, v147, s[0:1]
	v_cmp_lt_i32_e64 s[0:1], -1, v148
	v_fmac_f32_e32 v149, 0x3e0293ee, v129
	s_and_b64 s[0:1], s[0:1], vcc
	v_cndmask_b32_e64 v149, v241, v149, s[0:1]
	v_cmp_lt_i32_e64 s[0:1], -1, v150
	v_fmac_f32_e32 v151, 0x3e0293ee, v122
	s_and_b64 s[0:1], s[0:1], vcc
	v_cndmask_b32_e64 v44, v241, v151, s[0:1]
	v_cmp_lt_i32_e64 s[0:1], -1, v152
	v_fmac_f32_e32 v153, 0x3e0293ee, v123
	s_and_b64 s[0:1], s[0:1], vcc
	v_cndmask_b32_e64 v45, v241, v153, s[0:1]
	v_cmp_lt_i32_e64 s[0:1], -1, v154
	v_fmac_f32_e32 v155, 0x3e0293ee, v124
	s_and_b64 s[0:1], s[0:1], vcc
	v_cndmask_b32_e64 v138, v241, v155, s[0:1]
	v_cmp_lt_i32_e64 s[0:1], -1, v156
	v_fmac_f32_e32 v157, 0x3e0293ee, v125
	s_and_b64 s[0:1], s[0:1], vcc
	v_cndmask_b32_e64 v141, v241, v157, s[0:1]
	v_cmp_lt_i32_e64 s[0:1], -1, v158
	v_fmac_f32_e32 v159, 0x3e0293ee, v118
	s_and_b64 s[0:1], s[0:1], vcc
	v_cndmask_b32_e64 v139, v241, v159, s[0:1]
	v_cmp_lt_i32_e64 s[0:1], -1, v160
	v_max_f32_e32 v42, v5, v38
	v_fmac_f32_e32 v161, 0x3e0293ee, v119
	s_and_b64 s[0:1], s[0:1], vcc
	v_max3_f32 v42, v42, v39, v41
	v_cndmask_b32_e64 v146, v241, v161, s[0:1]
	v_cmp_lt_i32_e64 s[0:1], -1, v162
	v_max3_f32 v42, v42, v40, v140
	v_fmac_f32_e32 v163, 0x3e0293ee, v120
	s_and_b64 s[0:1], s[0:1], vcc
	v_max3_f32 v42, v42, v147, v149
	v_cndmask_b32_e64 v148, v241, v163, s[0:1]
	v_cmp_lt_i32_e64 s[0:1], -1, v164
	v_max3_f32 v42, v42, v44, v45
	v_fmac_f32_e32 v165, 0x3e0293ee, v121
	s_and_b64 vcc, s[0:1], vcc
	v_max3_f32 v42, v42, v138, v141
	v_cndmask_b32_e32 v150, v241, v165, vcc
	v_max3_f32 v42, v42, v139, v146
	v_max3_f32 v42, v42, v148, v150
	v_add_f32_e32 v43, 0x41000000, v136
	v_cmp_gt_f32_e32 vcc, v42, v43
	s_cbranch_vccz .LBB0_1140
	ds_bpermute_b32 v43, v245, v42
	v_max_f32_e32 v42, v42, v42
	s_waitcnt lgkmcnt(0)
	v_max_f32_e32 v43, v43, v43
	v_max_f32_e32 v42, v42, v43
	ds_bpermute_b32 v43, v246, v42
	s_waitcnt lgkmcnt(0)
	v_max3_f32 v42, v136, v42, v43
	v_sub_f32_e32 v43, v136, v42
	v_exp_f32_e32 v194, v43
	v_mov_b32_e32 v43, v137
	v_mov_b64_e32 v[204:205], v[42:43]
	s_branch .LBB0_1141

.LBB0_1192:
	s_mov_b32 s98, 0x26000
	v_lshl_add_u32 v118, v0, 4, s98
	ds_read_b128 v[118:121], v118
	s_andn2_b64 vcc, exec, s[6:7]
	s_cbranch_vccnz .LBB0_1194
	s_waitcnt vmcnt(4)

.LBB0_1202:
	s_mul_hi_u32 s6, s45, 0xaaaaaaab
	s_lshr_b32 s6, s6, 1
	s_mul_i32 s6, s6, 0x18000
	s_sub_i32 s35, s64, s6
	s_sub_i32 s19, s80, s6
	s_sub_i32 s38, s79, s6
	s_sub_i32 s39, s58, s6
	s_mul_i32 s6, s18, s42
	s_lshl_b32 s6, s6, 1
	s_add_u32 s98, s36, s6
	s_addc_u32 s99, s37, 0
	s_lshl_b32 s6, s18, 1
	s_add_u32 s100, s20, s6
	s_addc_u32 s101, s21, 0
	s_add_i32 s6, s47, s39
	s_add_i32 m0, s15, s6
	s_waitcnt lgkmcnt(0)
	global_load_lds_dwordx4 v118, s[98:99]
	s_add_i32 s6, s47, s19
	s_add_i32 m0, s15, s6
	s_nop 0
	global_load_lds_dwordx4 v119, s[98:99]
	s_add_i32 s18, s47, s38
	s_add_i32 m0, s15, s18
	s_nop 0
	global_load_lds_dwordx4 v120, s[100:101]
	s_add_i32 s6, s47, s35
	s_add_i32 m0, s15, s6
	s_nop 0
	global_load_lds_dwordx4 v121, s[100:101]
.LBB0_1203:
	s_waitcnt lgkmcnt(0)
	s_add_i32 s34, s10, 63
	s_cmp_le_i32 s10, s9
	s_cselect_b64 s[6:7], -1, 0
	s_cmp_ge_i32 s34, s17
	s_cselect_b64 s[18:19], -1, 0
	s_and_b64 s[18:19], s[6:7], s[18:19]
	s_cmp_le_i32 s10, s8
	s_cselect_b64 s[20:21], -1, 0
	s_cmp_ge_i32 s34, s44
	s_cselect_b64 s[6:7], -1, 0
	s_and_b64 s[36:37], s[20:21], s[6:7]
	s_or_b64 s[20:21], s[18:19], s[36:37]
	s_andn2_b64 vcc, exec, s[20:21]
	s_cbranch_vccnz .LBB0_1209
	s_mul_hi_u32 s20, s13, 0xaaaaaaab
	s_lshr_b32 s42, s20, 1
	s_and_b64 s[6:7], s[18:19], s[6:7]
	s_add_i32 s20, s14, 0xffffffba
	s_cmpk_gt_i32 s20, 0x7e
	s_cselect_b64 s[34:35], -1, 0
	s_and_b64 s[6:7], s[34:35], s[6:7]
	s_cmpk_lt_i32 s14, 0x200
	s_cselect_b64 s[20:21], -1, 0
	s_mul_i32 s42, s42, 0x18000
	s_and_b64 s[38:39], s[6:7], s[20:21]
	v_cndmask_b32_e64 v5, 0, 1, s[18:19]
	v_subrev_u32_e32 v1, s42, v232
	v_subrev_u32_e32 v2, s42, v233
	v_subrev_u32_e32 v142, s42, v234
	v_subrev_u32_e32 v143, s42, v235
	s_mov_b64 s[6:7], -1
	s_andn2_b64 vcc, exec, s[38:39]
	v_cmp_ne_u32_e64 s[18:19], 1, v5
	s_cbranch_vccz .LBB0_1230
	s_and_b64 vcc, exec, s[18:19]
	v_mov_b64_e32 v[196:197], v[136:137]
	v_mov_b64_e32 v[198:199], v[134:135]
	s_cbranch_vccnz .LBB0_1217
	s_add_i32 s6, s15, s47
	v_add_u32_e32 v5, s6, v143
	v_add_u32_e32 v148, s6, v142
	v_add_u32_e32 v149, s6, v2
	v_add_u32_e32 v152, s6, v1
	ds_read_b128 v[38:41], v5
	ds_read_b128 v[42:45], v5 offset:4096
	ds_read_b128 v[118:121], v148
	ds_read_b128 v[122:125], v148 offset:4096
	ds_read_b128 v[126:129], v149
	ds_read_b128 v[138:141], v149 offset:4096
	ds_read_b128 v[130:133], v152
	ds_read_b128 v[144:147], v152 offset:4096
	s_setprio 1
	s_waitcnt lgkmcnt(0)
	v_mfma_f32_16x16x32_f16 v[38:41], v[38:41], v[6:9], 0
	v_mfma_f32_16x16x32_f16 v[38:41], v[118:121], v[10:13], v[38:41]
	v_mfma_f32_16x16x32_f16 v[38:41], v[126:129], v[14:17], v[38:41]
	v_mfma_f32_16x16x32_f16 v[130:133], v[130:133], v[18:21], v[38:41]
	v_mfma_f32_16x16x32_f16 v[38:41], v[42:45], v[6:9], 0
	v_mfma_f32_16x16x32_f16 v[38:41], v[122:125], v[10:13], v[38:41]
	v_mfma_f32_16x16x32_f16 v[38:41], v[138:141], v[14:17], v[38:41]
	v_mfma_f32_16x16x32_f16 v[126:129], v[144:147], v[18:21], v[38:41]
	s_setprio 0
	s_nop 5
	ds_read_b128 v[38:41], v5 offset:8192
	ds_read_b128 v[42:45], v5 offset:12288
	ds_read_b128 v[118:121], v148 offset:8192
	ds_read_b128 v[138:141], v148 offset:12288
	ds_read_b128 v[122:125], v149 offset:8192
	ds_read_b128 v[144:147], v149 offset:12288
	ds_read_b128 v[148:151], v152 offset:8192
	ds_read_b128 v[152:155], v152 offset:12288
	s_setprio 1
	s_waitcnt lgkmcnt(0)
	v_mfma_f32_16x16x32_f16 v[38:41], v[38:41], v[6:9], 0
	v_mfma_f32_16x16x32_f16 v[38:41], v[118:121], v[10:13], v[38:41]
	v_mfma_f32_16x16x32_f16 v[38:41], v[122:125], v[14:17], v[38:41]
	v_mfma_f32_16x16x32_f16 v[122:125], v[148:151], v[18:21], v[38:41]
	v_mfma_f32_16x16x32_f16 v[38:41], v[42:45], v[6:9], 0
	v_mfma_f32_16x16x32_f16 v[38:41], v[138:141], v[10:13], v[38:41]
	v_mfma_f32_16x16x32_f16 v[38:41], v[144:147], v[14:17], v[38:41]
	v_mfma_f32_16x16x32_f16 v[118:121], v[152:155], v[18:21], v[38:41]
	s_setprio 0
	s_add_i32 s6, s14, -4
	s_cmpk_lt_i32 s6, 0x200
	s_cselect_b64 s[6:7], -1, 0
	s_and_b64 s[6:7], s[34:35], s[6:7]
	s_andn2_b64 vcc, exec, s[6:7]
	s_mov_b64 s[6:7], -1
	s_cbranch_vccz .LBB0_1212
	v_add_u32_e32 v5, s14, v239
	v_add_u32_e32 v38, -7, v5
	v_add_u32_e32 v40, -8, v5
	v_add_u32_e32 v42, -9, v5
	v_add_u32_e32 v44, -10, v5
	v_add_u32_e32 v138, -11, v5
	v_add_u32_e32 v140, -12, v5
	v_add_u32_e32 v144, -13, v5
	v_med3_i32 v39, v38, 0, v243
	v_med3_i32 v41, v40, 0, v243
	v_med3_i32 v43, v42, 0, v243
	v_med3_i32 v45, v44, 0, v243
	v_med3_i32 v139, v138, 0, v243
	v_med3_i32 v141, v140, 0, v243
	v_med3_i32 v145, v144, 0, v243
	v_add_u32_e32 v148, -14, v5
	v_lshl_add_u32 v39, v39, 2, v244
	v_lshl_add_u32 v41, v41, 2, v244
	v_lshl_add_u32 v43, v43, 2, v244
	v_lshl_add_u32 v45, v45, 2, v244
	v_lshl_add_u32 v139, v139, 2, v244
	v_lshl_add_u32 v141, v141, 2, v244
	v_lshl_add_u32 v145, v145, 2, v244
	v_med3_i32 v146, v148, 0, v243
	v_subrev_u32_e32 v150, 39, v5
	v_subrev_u32_e32 v152, 41, v5
	v_subrev_u32_e32 v154, 42, v5
	v_subrev_u32_e32 v156, 43, v5
	v_subrev_u32_e32 v158, 44, v5
	v_subrev_u32_e32 v160, 45, v5
	v_lshl_add_u32 v146, v146, 2, v244
	ds_read_b32 v39, v39
	ds_read_b32 v41, v41
	ds_read_b32 v43, v43
	ds_read_b32 v45, v45
	ds_read_b32 v139, v139
	ds_read_b32 v141, v141
	ds_read_b32 v147, v145
	ds_read_b32 v149, v146
	v_med3_i32 v145, v150, 0, v243
	v_subrev_u32_e32 v151, 40, v5
	v_med3_i32 v153, v152, 0, v243
	v_med3_i32 v155, v154, 0, v243
	v_med3_i32 v157, v156, 0, v243
	v_med3_i32 v159, v158, 0, v243
	v_med3_i32 v161, v160, 0, v243
	v_subrev_u32_e32 v162, 46, v5
	v_lshl_add_u32 v145, v145, 2, v244
	v_med3_i32 v146, v151, 0, v243
	v_lshl_add_u32 v153, v153, 2, v244
	v_lshl_add_u32 v155, v155, 2, v244
	v_lshl_add_u32 v157, v157, 2, v244
	v_lshl_add_u32 v159, v159, 2, v244
	v_lshl_add_u32 v161, v161, 2, v244
	v_med3_i32 v5, v162, 0, v243
	v_lshl_add_u32 v146, v146, 2, v244
	v_lshl_add_u32 v5, v5, 2, v244
	ds_read_b32 v163, v145
	ds_read_b32 v164, v146
	ds_read_b32 v153, v153
	ds_read_b32 v155, v155
	ds_read_b32 v157, v157
	ds_read_b32 v159, v159
	ds_read_b32 v161, v161
	ds_read_b32 v165, v5
	s_waitcnt lgkmcnt(0)
	v_fmac_f32_e32 v39, 0x3e0293ee, v130
	v_cmp_gt_u32_e32 vcc, s62, v38
	v_fmac_f32_e32 v41, 0x3e0293ee, v131
	v_fmac_f32_e32 v43, 0x3e0293ee, v132
	v_cndmask_b32_e32 v38, v241, v39, vcc
	v_cmp_gt_u32_e32 vcc, s62, v40
	v_fmac_f32_e32 v45, 0x3e0293ee, v133
	v_fmac_f32_e32 v139, 0x3e0293ee, v126
	v_cndmask_b32_e32 v39, v241, v41, vcc
	v_cmp_gt_u32_e32 vcc, s62, v42
	v_fmac_f32_e32 v141, 0x3e0293ee, v127
	v_fmac_f32_e32 v147, 0x3e0293ee, v128
	v_cndmask_b32_e32 v41, v241, v43, vcc
	v_cmp_gt_u32_e32 vcc, s62, v44
	v_fmac_f32_e32 v149, 0x3e0293ee, v129
	v_fmac_f32_e32 v163, 0x3e0293ee, v122
	v_cndmask_b32_e32 v146, v241, v45, vcc
	v_cmp_gt_u32_e32 vcc, s62, v138
	v_fmac_f32_e32 v164, 0x3e0293ee, v123
	v_fmac_f32_e32 v153, 0x3e0293ee, v124
	v_cndmask_b32_e32 v40, v241, v139, vcc
	v_cmp_gt_u32_e32 vcc, s62, v140
	v_max_f32_e32 v42, v38, v39
	v_fmac_f32_e32 v155, 0x3e0293ee, v125
	v_cndmask_b32_e32 v145, v241, v141, vcc
	v_cmp_gt_u32_e32 vcc, s62, v144
	v_max3_f32 v42, v42, v41, v146
	v_fmac_f32_e32 v157, 0x3e0293ee, v118
	v_cndmask_b32_e32 v147, v241, v147, vcc
	v_cmp_gt_u32_e32 vcc, s62, v148
	v_max3_f32 v42, v42, v40, v145
	v_fmac_f32_e32 v159, 0x3e0293ee, v119
	v_cndmask_b32_e32 v148, v241, v149, vcc
	v_cmp_gt_u32_e32 vcc, s62, v150
	v_max3_f32 v42, v42, v147, v148
	v_fmac_f32_e32 v161, 0x3e0293ee, v120
	v_cndmask_b32_e32 v5, v241, v163, vcc
	v_cmp_gt_u32_e32 vcc, s62, v151
	v_fmac_f32_e32 v165, 0x3e0293ee, v121
	v_add_f32_e32 v43, 0x41000000, v136
	v_cndmask_b32_e32 v44, v241, v164, vcc
	v_cmp_gt_u32_e32 vcc, s62, v152
	v_max3_f32 v42, v42, v5, v44
	s_nop 0
	v_cndmask_b32_e32 v138, v241, v153, vcc
	v_cmp_gt_u32_e32 vcc, s62, v154
	s_nop 1
	v_cndmask_b32_e32 v140, v241, v155, vcc
	v_cmp_gt_u32_e32 vcc, s62, v156
	v_max3_f32 v42, v42, v138, v140
	s_nop 0
	v_cndmask_b32_e32 v45, v241, v157, vcc
	v_cmp_gt_u32_e32 vcc, s62, v158
	s_nop 1
	v_cndmask_b32_e32 v139, v241, v159, vcc
	v_cmp_gt_u32_e32 vcc, s62, v160
	v_max3_f32 v42, v42, v45, v139
	s_nop 0
	v_cndmask_b32_e32 v141, v241, v161, vcc
	v_cmp_gt_u32_e32 vcc, s62, v162
	s_nop 1
	v_cndmask_b32_e32 v144, v241, v165, vcc
	v_max3_f32 v42, v42, v141, v144
	v_cmp_gt_f32_e32 vcc, v42, v43
	s_cbranch_vccz .LBB0_1210
	ds_bpermute_b32 v43, v245, v42
	v_max_f32_e32 v42, v42, v42
	s_waitcnt lgkmcnt(0)
	v_max_f32_e32 v43, v43, v43
	v_max_f32_e32 v42, v42, v43
	ds_bpermute_b32 v43, v246, v42
	s_waitcnt lgkmcnt(0)
	v_max3_f32 v42, v136, v42, v43
	v_sub_f32_e32 v43, v136, v42
	v_exp_f32_e32 v194, v43
	v_mov_b32_e32 v43, v137
	v_mov_b64_e32 v[196:197], v[42:43]
	s_branch .LBB0_1211
